# as v72 plus the SwiGLU output scale folded into the sigmoid denominator (fma instead of add, one mul fewer per element) in both the dense FFN-up and MoE-up fp8 epilogues
# speedup vs baseline: 1.0124x; 1.0072x over previous
.LBB0_761:
	v_mul_f32_e32 v146, 0xbfb8aa3b, v126
	v_exp_f32_e32 v157, v146
	v_mul_f32_e32 v158, 0xbfb8aa3b, v127
	v_exp_f32_e32 v160, v158
	v_lshl_add_u32 v156, s24, 8, v1
	s_mov_b32 s98, 0x3e000000
	v_fma_f32 v157, v157, s98, s98
	v_rcp_f32_e32 v157, v157
	v_fma_f32 v160, v160, s98, s98
	v_rcp_f32_e32 v160, v160
	v_lshl_or_b32 v146, s48, 7, v151
	v_mul_f32_e32 v126, v126, v157
	v_mul_f32_e32 v118, v126, v118
	v_mul_f32_e32 v126, v127, v160
	v_mul_f32_e32 v127, 0xbfb8aa3b, v128
	v_exp_f32_e32 v127, v127
	v_mul_f32_e32 v157, 0xbfb8aa3b, v129
	v_exp_f32_e32 v157, v157
	v_fma_f32 v127, v127, s98, s98
	v_rcp_f32_e32 v127, v127
	v_mul_f32_e32 v119, v126, v119
	v_fma_f32 v126, v157, s98, s98
	v_rcp_f32_e32 v126, v126
	v_mul_f32_e32 v127, v128, v127
	v_mul_f32_e32 v120, v127, v120
	v_mul_f32_e32 v127, 0xbfb8aa3b, v122
	v_exp_f32_e32 v127, v127
	v_mul_f32_e32 v128, 0xbfb8aa3b, v123
	v_exp_f32_e32 v128, v128
	v_mul_f32_e32 v126, v129, v126
	v_fma_f32 v127, v127, s98, s98
	v_rcp_f32_e32 v127, v127
	v_mul_f32_e32 v121, v126, v121
	v_fma_f32 v126, v128, s98, s98
	v_rcp_f32_e32 v126, v126
	v_mul_f32_e32 v122, v122, v127
	v_mul_f32_e32 v122, v122, v114
	v_mul_f32_e32 v114, v123, v126
	v_mul_f32_e32 v126, 0xbfb8aa3b, v125
	v_exp_f32_e32 v126, v126
	v_mul_f32_e32 v123, 0xbfb8aa3b, v124
	v_exp_f32_e32 v123, v123
	v_mul_f32_e32 v115, v114, v115
	v_fma_f32 v114, v126, s98, s98
	v_rcp_f32_e32 v114, v114
	v_fma_f32 v123, v123, s98, s98
	v_rcp_f32_e32 v123, v123
	v_med3_f32 v118, v118, s47, v155
	v_mul_f32_e32 v114, v125, v114
	v_mul_f32_e32 v117, v114, v117
	v_med3_f32 v119, v119, s47, v155
	v_mov_b32_e32 v114, 0
	v_cvt_pk_fp8_f32 v114, v118, v119
	v_med3_f32 v118, v122, s47, v155
	v_med3_f32 v119, v115, s47, v155
	v_mov_b32_e32 v115, 0
	v_mul_f32_e32 v123, v124, v123
	v_cvt_pk_fp8_f32 v115, v118, v119
	v_mul_f32_e32 v116, v123, v116
	v_med3_f32 v120, v120, s47, v155
	v_med3_f32 v121, v121, s47, v155
	v_med3_f32 v116, v116, s47, v155
	v_med3_f32 v117, v117, s47, v155
	v_cvt_pk_fp8_f32 v114, v120, v121 op_sel:[0,0,1]
	v_cvt_pk_fp8_f32 v115, v116, v117 op_sel:[0,0,1]
	v_mov_b64_e32 v[148:149], s[10:11]
	v_ashrrev_i32_e32 v147, 31, v146
	v_mad_i64_i32 v[158:159], s[26:27], v156, s46, v[148:149]
	v_mul_f32_e32 v116, 0xbfb8aa3b, v110
	v_exp_f32_e32 v118, v116
	v_lshl_add_u64 v[116:117], v[158:159], 0, v[146:147]
	global_store_dwordx2 v[116:117], v[114:115], off
	v_mul_f32_e32 v116, 0xbfb8aa3b, v111
	v_exp_f32_e32 v116, v116
	v_fma_f32 v115, v118, s98, s98
	v_rcp_f32_e32 v117, v115
	v_or_b32_e32 v114, 16, v156
	v_fma_f32 v116, v116, s98, s98
	v_rcp_f32_e32 v116, v116
	v_mul_f32_e32 v110, v110, v117
	v_mul_f32_e32 v102, v110, v102
	v_mul_f32_e32 v110, v111, v116
	v_mul_f32_e32 v111, 0xbfb8aa3b, v112
	v_exp_f32_e32 v111, v111
	v_mul_f32_e32 v116, 0xbfb8aa3b, v113
	v_exp_f32_e32 v116, v116
	v_fma_f32 v111, v111, s98, s98
	v_rcp_f32_e32 v111, v111
	v_mul_f32_e32 v103, v110, v103
	v_fma_f32 v110, v116, s98, s98
	v_rcp_f32_e32 v110, v110
	v_mul_f32_e32 v111, v112, v111
	v_mul_f32_e32 v104, v111, v104
	v_mul_f32_e32 v111, 0xbfb8aa3b, v106
	v_exp_f32_e32 v111, v111
	v_mul_f32_e32 v112, 0xbfb8aa3b, v107
	v_exp_f32_e32 v112, v112
	v_mul_f32_e32 v110, v113, v110
	v_fma_f32 v111, v111, s98, s98
	v_rcp_f32_e32 v111, v111
	v_mul_f32_e32 v105, v110, v105
	v_fma_f32 v110, v112, s98, s98
	v_rcp_f32_e32 v110, v110
	v_mul_f32_e32 v106, v106, v111
	v_mul_f32_e32 v106, v106, v98
	v_mul_f32_e32 v98, v107, v110
	v_mul_f32_e32 v110, 0xbfb8aa3b, v109
	v_exp_f32_e32 v110, v110
	v_mul_f32_e32 v107, 0xbfb8aa3b, v108
	v_exp_f32_e32 v107, v107
	v_mul_f32_e32 v99, v98, v99
	v_fma_f32 v98, v110, s98, s98
	v_rcp_f32_e32 v98, v98
	v_fma_f32 v107, v107, s98, s98
	v_rcp_f32_e32 v107, v107
	v_med3_f32 v102, v102, s47, v155
	v_mul_f32_e32 v98, v109, v98
	v_mul_f32_e32 v101, v98, v101
	v_med3_f32 v103, v103, s47, v155
	v_mov_b32_e32 v98, 0
	v_cvt_pk_fp8_f32 v98, v102, v103
	v_med3_f32 v102, v106, s47, v155
	v_med3_f32 v103, v99, s47, v155
	v_mov_b32_e32 v99, 0
	v_mul_f32_e32 v107, v108, v107
	v_cvt_pk_fp8_f32 v99, v102, v103
	v_mul_f32_e32 v100, v107, v100
	v_med3_f32 v104, v104, s47, v155
	v_med3_f32 v105, v105, s47, v155
	v_med3_f32 v100, v100, s47, v155
	v_med3_f32 v101, v101, s47, v155
	v_cvt_pk_fp8_f32 v98, v104, v105 op_sel:[0,0,1]
	v_cvt_pk_fp8_f32 v99, v100, v101 op_sel:[0,0,1]
	v_mad_i64_i32 v[114:115], s[26:27], v114, s46, v[148:149]
	v_mul_f32_e32 v100, 0xbfb8aa3b, v94
	v_exp_f32_e32 v102, v100
	v_lshl_add_u64 v[100:101], v[114:115], 0, v[146:147]
	global_store_dwordx2 v[100:101], v[98:99], off
	v_mul_f32_e32 v100, 0xbfb8aa3b, v95
	v_exp_f32_e32 v100, v100
	v_fma_f32 v99, v102, s98, s98
	v_rcp_f32_e32 v101, v99
	v_or_b32_e32 v98, 32, v156
	v_fma_f32 v100, v100, s98, s98
	v_rcp_f32_e32 v100, v100
	v_mul_f32_e32 v94, v94, v101
	v_mul_f32_e32 v86, v94, v86
	v_mul_f32_e32 v94, v95, v100
	v_mul_f32_e32 v95, 0xbfb8aa3b, v96
	v_exp_f32_e32 v95, v95
	v_mul_f32_e32 v100, 0xbfb8aa3b, v97
	v_exp_f32_e32 v100, v100
	v_fma_f32 v95, v95, s98, s98
	v_rcp_f32_e32 v95, v95
	v_mul_f32_e32 v87, v94, v87
	v_fma_f32 v94, v100, s98, s98
	v_rcp_f32_e32 v94, v94
	v_mul_f32_e32 v95, v96, v95
	v_mul_f32_e32 v88, v95, v88
	v_mul_f32_e32 v95, 0xbfb8aa3b, v90
	v_exp_f32_e32 v95, v95
	v_mul_f32_e32 v96, 0xbfb8aa3b, v91
	v_exp_f32_e32 v96, v96
	v_mul_f32_e32 v94, v97, v94
	v_fma_f32 v95, v95, s98, s98
	v_rcp_f32_e32 v95, v95
	v_mul_f32_e32 v89, v94, v89
	v_fma_f32 v94, v96, s98, s98
	v_rcp_f32_e32 v94, v94
	v_mul_f32_e32 v90, v90, v95
	v_mul_f32_e32 v90, v90, v82
	v_mul_f32_e32 v82, v91, v94
	v_mul_f32_e32 v94, 0xbfb8aa3b, v93
	v_exp_f32_e32 v94, v94
	v_mul_f32_e32 v91, 0xbfb8aa3b, v92
	v_exp_f32_e32 v91, v91
	v_mul_f32_e32 v83, v82, v83
	v_fma_f32 v82, v94, s98, s98
	v_rcp_f32_e32 v82, v82
	v_fma_f32 v91, v91, s98, s98
	v_rcp_f32_e32 v91, v91
	v_med3_f32 v86, v86, s47, v155
	v_mul_f32_e32 v82, v93, v82
	v_mul_f32_e32 v85, v82, v85
	v_med3_f32 v87, v87, s47, v155
	v_mov_b32_e32 v82, 0
	v_cvt_pk_fp8_f32 v82, v86, v87
	v_med3_f32 v86, v90, s47, v155
	v_med3_f32 v87, v83, s47, v155
	v_mov_b32_e32 v83, 0
	v_mul_f32_e32 v91, v92, v91
	v_cvt_pk_fp8_f32 v83, v86, v87
	v_mul_f32_e32 v84, v91, v84
	v_med3_f32 v88, v88, s47, v155
	v_med3_f32 v89, v89, s47, v155
	v_med3_f32 v84, v84, s47, v155
	v_med3_f32 v85, v85, s47, v155
	v_cvt_pk_fp8_f32 v82, v88, v89 op_sel:[0,0,1]
	v_cvt_pk_fp8_f32 v83, v84, v85 op_sel:[0,0,1]
	v_mad_i64_i32 v[98:99], s[26:27], v98, s46, v[148:149]
	v_mul_f32_e32 v84, 0xbfb8aa3b, v78
	v_exp_f32_e32 v86, v84
	v_lshl_add_u64 v[84:85], v[98:99], 0, v[146:147]
	global_store_dwordx2 v[84:85], v[82:83], off
	v_mul_f32_e32 v84, 0xbfb8aa3b, v79
	v_exp_f32_e32 v84, v84
	v_fma_f32 v83, v86, s98, s98
	v_rcp_f32_e32 v85, v83
	v_or_b32_e32 v82, 48, v156
	v_fma_f32 v84, v84, s98, s98
	v_rcp_f32_e32 v84, v84
	v_mul_f32_e32 v78, v78, v85
	v_mul_f32_e32 v70, v78, v70
	v_mul_f32_e32 v78, v79, v84
	v_mul_f32_e32 v79, 0xbfb8aa3b, v80
	v_exp_f32_e32 v79, v79
	v_mul_f32_e32 v84, 0xbfb8aa3b, v81
	v_exp_f32_e32 v84, v84
	v_fma_f32 v79, v79, s98, s98
	v_rcp_f32_e32 v79, v79
	v_mul_f32_e32 v71, v78, v71
	v_fma_f32 v78, v84, s98, s98
	v_rcp_f32_e32 v78, v78
	v_mul_f32_e32 v79, v80, v79
	v_mul_f32_e32 v72, v79, v72
	v_mul_f32_e32 v79, 0xbfb8aa3b, v74
	v_exp_f32_e32 v79, v79
	v_mul_f32_e32 v80, 0xbfb8aa3b, v75
	v_exp_f32_e32 v80, v80
	v_mul_f32_e32 v78, v81, v78
	v_fma_f32 v79, v79, s98, s98
	v_rcp_f32_e32 v79, v79
	v_mul_f32_e32 v73, v78, v73
	v_fma_f32 v78, v80, s98, s98
	v_rcp_f32_e32 v78, v78
	v_mul_f32_e32 v74, v74, v79
	v_mul_f32_e32 v74, v74, v66
	v_mul_f32_e32 v66, v75, v78
	v_mul_f32_e32 v78, 0xbfb8aa3b, v77
	v_exp_f32_e32 v78, v78
	v_mul_f32_e32 v75, 0xbfb8aa3b, v76
	v_exp_f32_e32 v75, v75
	v_mul_f32_e32 v67, v66, v67
	v_fma_f32 v66, v78, s98, s98
	v_rcp_f32_e32 v66, v66
	v_fma_f32 v75, v75, s98, s98
	v_rcp_f32_e32 v75, v75
	v_med3_f32 v70, v70, s47, v155
	v_mul_f32_e32 v66, v77, v66
	v_mul_f32_e32 v69, v66, v69
	v_med3_f32 v71, v71, s47, v155
	v_mov_b32_e32 v66, 0
	v_cvt_pk_fp8_f32 v66, v70, v71
	v_med3_f32 v70, v74, s47, v155
	v_med3_f32 v71, v67, s47, v155
	v_mov_b32_e32 v67, 0
	v_mul_f32_e32 v75, v76, v75
	v_cvt_pk_fp8_f32 v67, v70, v71
	v_mul_f32_e32 v68, v75, v68
	v_med3_f32 v72, v72, s47, v155
	v_med3_f32 v73, v73, s47, v155
	v_med3_f32 v68, v68, s47, v155
	v_med3_f32 v69, v69, s47, v155
	v_cvt_pk_fp8_f32 v66, v72, v73 op_sel:[0,0,1]
	v_cvt_pk_fp8_f32 v67, v68, v69 op_sel:[0,0,1]
	v_mad_i64_i32 v[82:83], s[26:27], v82, s46, v[148:149]
	v_mul_f32_e32 v68, 0xbfb8aa3b, v62
	v_exp_f32_e32 v70, v68
	v_lshl_add_u64 v[68:69], v[82:83], 0, v[146:147]
	global_store_dwordx2 v[68:69], v[66:67], off
	v_mul_f32_e32 v68, 0xbfb8aa3b, v63
	v_exp_f32_e32 v68, v68
	v_fma_f32 v67, v70, s98, s98
	v_rcp_f32_e32 v69, v67
	v_add_u32_e32 v66, 0x80, v156
	v_fma_f32 v68, v68, s98, s98
	v_rcp_f32_e32 v68, v68
	v_mul_f32_e32 v62, v62, v69
	v_mul_f32_e32 v54, v62, v54
	v_mul_f32_e32 v62, v63, v68
	v_mul_f32_e32 v63, 0xbfb8aa3b, v64
	v_exp_f32_e32 v63, v63
	v_mul_f32_e32 v68, 0xbfb8aa3b, v65
	v_exp_f32_e32 v68, v68
	v_fma_f32 v63, v63, s98, s98
	v_rcp_f32_e32 v63, v63
	v_mul_f32_e32 v55, v62, v55
	v_fma_f32 v62, v68, s98, s98
	v_rcp_f32_e32 v62, v62
	v_mul_f32_e32 v63, v64, v63
	v_mul_f32_e32 v56, v63, v56
	v_mul_f32_e32 v63, 0xbfb8aa3b, v58
	v_exp_f32_e32 v63, v63
	v_mul_f32_e32 v64, 0xbfb8aa3b, v59
	v_exp_f32_e32 v64, v64
	v_mul_f32_e32 v62, v65, v62
	v_fma_f32 v63, v63, s98, s98
	v_rcp_f32_e32 v63, v63
	v_mul_f32_e32 v57, v62, v57
	v_fma_f32 v62, v64, s98, s98
	v_rcp_f32_e32 v62, v62
	v_mul_f32_e32 v58, v58, v63
	v_mul_f32_e32 v58, v58, v50
	v_mul_f32_e32 v50, v59, v62
	v_mul_f32_e32 v62, 0xbfb8aa3b, v61
	v_exp_f32_e32 v62, v62
	v_mul_f32_e32 v59, 0xbfb8aa3b, v60
	v_exp_f32_e32 v59, v59
	v_mul_f32_e32 v51, v50, v51
	v_fma_f32 v50, v62, s98, s98
	v_rcp_f32_e32 v50, v50
	v_fma_f32 v59, v59, s98, s98
	v_rcp_f32_e32 v59, v59
	v_med3_f32 v54, v54, s47, v155
	v_mul_f32_e32 v50, v61, v50
	v_mul_f32_e32 v53, v50, v53
	v_med3_f32 v55, v55, s47, v155
	v_mov_b32_e32 v50, 0
	v_cvt_pk_fp8_f32 v50, v54, v55
	v_med3_f32 v54, v58, s47, v155
	v_med3_f32 v55, v51, s47, v155
	v_mov_b32_e32 v51, 0
	v_mul_f32_e32 v59, v60, v59
	v_cvt_pk_fp8_f32 v51, v54, v55
	v_mul_f32_e32 v52, v59, v52
	v_med3_f32 v56, v56, s47, v155
	v_med3_f32 v57, v57, s47, v155
	v_med3_f32 v52, v52, s47, v155
	v_med3_f32 v53, v53, s47, v155
	v_cvt_pk_fp8_f32 v50, v56, v57 op_sel:[0,0,1]
	v_cvt_pk_fp8_f32 v51, v52, v53 op_sel:[0,0,1]
	v_mad_i64_i32 v[66:67], s[26:27], v66, s46, v[148:149]
	v_mul_f32_e32 v52, 0xbfb8aa3b, v46
	v_exp_f32_e32 v54, v52
	v_lshl_add_u64 v[52:53], v[66:67], 0, v[146:147]
	global_store_dwordx2 v[52:53], v[50:51], off
	v_mul_f32_e32 v52, 0xbfb8aa3b, v47
	v_exp_f32_e32 v52, v52
	v_fma_f32 v51, v54, s98, s98
	v_rcp_f32_e32 v53, v51
	v_add_u32_e32 v50, 0x90, v156
	v_fma_f32 v52, v52, s98, s98
	v_rcp_f32_e32 v52, v52
	v_mul_f32_e32 v46, v46, v53
	v_mul_f32_e32 v38, v46, v38
	v_mul_f32_e32 v46, v47, v52
	v_mul_f32_e32 v47, 0xbfb8aa3b, v48
	v_exp_f32_e32 v47, v47
	v_mul_f32_e32 v52, 0xbfb8aa3b, v49
	v_exp_f32_e32 v52, v52
	v_fma_f32 v47, v47, s98, s98
	v_rcp_f32_e32 v47, v47
	v_mul_f32_e32 v39, v46, v39
	v_fma_f32 v46, v52, s98, s98
	v_rcp_f32_e32 v46, v46
	v_mul_f32_e32 v47, v48, v47
	v_mul_f32_e32 v40, v47, v40
	v_mul_f32_e32 v47, 0xbfb8aa3b, v42
	v_exp_f32_e32 v47, v47
	v_mul_f32_e32 v48, 0xbfb8aa3b, v43
	v_exp_f32_e32 v48, v48
	v_mul_f32_e32 v46, v49, v46
	v_fma_f32 v47, v47, s98, s98
	v_rcp_f32_e32 v47, v47
	v_mul_f32_e32 v41, v46, v41
	v_fma_f32 v46, v48, s98, s98
	v_rcp_f32_e32 v46, v46
	v_mul_f32_e32 v42, v42, v47
	v_mul_f32_e32 v42, v42, v34
	v_mul_f32_e32 v34, v43, v46
	v_mul_f32_e32 v46, 0xbfb8aa3b, v45
	v_exp_f32_e32 v46, v46
	v_mul_f32_e32 v43, 0xbfb8aa3b, v44
	v_exp_f32_e32 v43, v43
	v_mul_f32_e32 v35, v34, v35
	v_fma_f32 v34, v46, s98, s98
	v_rcp_f32_e32 v34, v34
	v_fma_f32 v43, v43, s98, s98
	v_rcp_f32_e32 v43, v43
	v_med3_f32 v38, v38, s47, v155
	v_mul_f32_e32 v34, v45, v34
	v_mul_f32_e32 v37, v34, v37
	v_med3_f32 v39, v39, s47, v155
	v_mov_b32_e32 v34, 0
	v_cvt_pk_fp8_f32 v34, v38, v39
	v_med3_f32 v38, v42, s47, v155
	v_med3_f32 v39, v35, s47, v155
	v_mov_b32_e32 v35, 0
	v_mul_f32_e32 v43, v44, v43
	v_cvt_pk_fp8_f32 v35, v38, v39
	v_mul_f32_e32 v36, v43, v36
	v_med3_f32 v40, v40, s47, v155
	v_med3_f32 v41, v41, s47, v155
	v_med3_f32 v36, v36, s47, v155
	v_med3_f32 v37, v37, s47, v155
	v_cvt_pk_fp8_f32 v34, v40, v41 op_sel:[0,0,1]
	v_cvt_pk_fp8_f32 v35, v36, v37 op_sel:[0,0,1]
	v_mad_i64_i32 v[50:51], s[26:27], v50, s46, v[148:149]
	v_mul_f32_e32 v36, 0xbfb8aa3b, v30
	v_exp_f32_e32 v38, v36
	v_lshl_add_u64 v[36:37], v[50:51], 0, v[146:147]
	global_store_dwordx2 v[36:37], v[34:35], off
	v_mul_f32_e32 v36, 0xbfb8aa3b, v31
	v_exp_f32_e32 v36, v36
	v_fma_f32 v35, v38, s98, s98
	v_rcp_f32_e32 v37, v35
	v_add_u32_e32 v34, 0xa0, v156
	v_fma_f32 v36, v36, s98, s98
	v_rcp_f32_e32 v36, v36
	v_mul_f32_e32 v30, v30, v37
	v_mul_f32_e32 v22, v30, v22
	v_mul_f32_e32 v30, v31, v36
	v_mul_f32_e32 v31, 0xbfb8aa3b, v32
	v_exp_f32_e32 v31, v31
	v_mul_f32_e32 v36, 0xbfb8aa3b, v33
	v_exp_f32_e32 v36, v36
	v_fma_f32 v31, v31, s98, s98
	v_rcp_f32_e32 v31, v31
	v_mul_f32_e32 v23, v30, v23
	v_fma_f32 v30, v36, s98, s98
	v_rcp_f32_e32 v30, v30
	v_mul_f32_e32 v31, v32, v31
	v_mul_f32_e32 v24, v31, v24
	v_mul_f32_e32 v31, 0xbfb8aa3b, v26
	v_exp_f32_e32 v31, v31
	v_mul_f32_e32 v32, 0xbfb8aa3b, v27
	v_exp_f32_e32 v32, v32
	v_mul_f32_e32 v30, v33, v30
	v_fma_f32 v31, v31, s98, s98
	v_rcp_f32_e32 v31, v31
	v_mul_f32_e32 v25, v30, v25
	v_fma_f32 v30, v32, s98, s98
	v_rcp_f32_e32 v30, v30
	v_mul_f32_e32 v26, v26, v31
	v_mul_f32_e32 v26, v26, v18
	v_mul_f32_e32 v18, v27, v30
	v_mul_f32_e32 v30, 0xbfb8aa3b, v29
	v_exp_f32_e32 v30, v30
	v_mul_f32_e32 v27, 0xbfb8aa3b, v28
	v_exp_f32_e32 v27, v27
	v_mul_f32_e32 v19, v18, v19
	v_fma_f32 v18, v30, s98, s98
	v_rcp_f32_e32 v18, v18
	v_fma_f32 v27, v27, s98, s98
	v_rcp_f32_e32 v27, v27
	v_med3_f32 v22, v22, s47, v155
	v_mul_f32_e32 v18, v29, v18
	v_mul_f32_e32 v21, v18, v21
	v_med3_f32 v23, v23, s47, v155
	v_mov_b32_e32 v18, 0
	v_cvt_pk_fp8_f32 v18, v22, v23
	v_med3_f32 v22, v26, s47, v155
	v_med3_f32 v23, v19, s47, v155
	v_mov_b32_e32 v19, 0
	v_mul_f32_e32 v27, v28, v27
	v_cvt_pk_fp8_f32 v19, v22, v23
	v_mul_f32_e32 v20, v27, v20
	v_med3_f32 v24, v24, s47, v155
	v_med3_f32 v25, v25, s47, v155
	v_med3_f32 v20, v20, s47, v155
	v_med3_f32 v21, v21, s47, v155
	v_cvt_pk_fp8_f32 v18, v24, v25 op_sel:[0,0,1]
	v_cvt_pk_fp8_f32 v19, v20, v21 op_sel:[0,0,1]
	v_mad_i64_i32 v[34:35], s[26:27], v34, s46, v[148:149]
	v_mul_f32_e32 v22, 0xbfb8aa3b, v14
	v_lshl_add_u64 v[20:21], v[34:35], 0, v[146:147]
	v_exp_f32_e32 v22, v22
	global_store_dwordx2 v[20:21], v[18:19], off
	v_mul_f32_e32 v18, 0xbfb8aa3b, v15
	v_exp_f32_e32 v18, v18
	v_fma_f32 v19, v22, s98, s98
	v_rcp_f32_e32 v19, v19
	v_add_u32_e32 v20, 0xb0, v156
	v_fma_f32 v18, v18, s98, s98
	v_rcp_f32_e32 v18, v18
	v_mul_f32_e32 v14, v14, v19
	v_mul_f32_e32 v6, v14, v6
	v_mul_f32_e32 v14, v15, v18
	v_mul_f32_e32 v15, 0xbfb8aa3b, v16
	v_exp_f32_e32 v15, v15
	v_mul_f32_e32 v18, 0xbfb8aa3b, v17
	v_exp_f32_e32 v18, v18
	v_fma_f32 v15, v15, s98, s98
	v_rcp_f32_e32 v15, v15
	v_mul_f32_e32 v7, v14, v7
	v_fma_f32 v14, v18, s98, s98
	v_rcp_f32_e32 v14, v14
	v_mul_f32_e32 v15, v16, v15
	v_mul_f32_e32 v8, v15, v8
	v_mul_f32_e32 v15, 0xbfb8aa3b, v10
	v_exp_f32_e32 v15, v15
	v_mul_f32_e32 v16, 0xbfb8aa3b, v11
	v_exp_f32_e32 v16, v16
	v_mul_f32_e32 v14, v17, v14
	v_fma_f32 v15, v15, s98, s98
	v_rcp_f32_e32 v15, v15
	v_mul_f32_e32 v9, v14, v9
	v_fma_f32 v14, v16, s98, s98
	v_rcp_f32_e32 v14, v14
	v_mul_f32_e32 v10, v10, v15
	v_mul_f32_e32 v10, v10, v2
	v_mul_f32_e32 v2, v11, v14
	v_mul_f32_e32 v14, 0xbfb8aa3b, v13
	v_exp_f32_e32 v14, v14
	v_mul_f32_e32 v11, 0xbfb8aa3b, v12
	v_exp_f32_e32 v11, v11
	v_mul_f32_e32 v3, v2, v3
	v_fma_f32 v2, v14, s98, s98
	v_rcp_f32_e32 v2, v2
	v_fma_f32 v11, v11, s98, s98
	v_rcp_f32_e32 v11, v11
	v_med3_f32 v6, v6, s47, v155
	v_mul_f32_e32 v2, v13, v2
	v_mul_f32_e32 v5, v2, v5
	v_med3_f32 v7, v7, s47, v155
	v_mov_b32_e32 v2, 0
	v_cvt_pk_fp8_f32 v2, v6, v7
	v_med3_f32 v6, v10, s47, v155
	v_med3_f32 v7, v3, s47, v155
	v_mov_b32_e32 v3, 0
	v_mul_f32_e32 v11, v12, v11
	v_cvt_pk_fp8_f32 v3, v6, v7
	v_mul_f32_e32 v4, v11, v4
	v_med3_f32 v8, v8, s47, v155
	v_med3_f32 v9, v9, s47, v155
	v_med3_f32 v4, v4, s47, v155
	v_med3_f32 v5, v5, s47, v155
	v_cvt_pk_fp8_f32 v2, v8, v9 op_sel:[0,0,1]
	v_cvt_pk_fp8_f32 v3, v4, v5 op_sel:[0,0,1]
	v_mad_i64_i32 v[4:5], s[26:27], v20, s46, v[148:149]
	v_lshl_add_u64 v[4:5], v[4:5], 0, v[146:147]
	s_andn2_b64 vcc, exec, s[6:7]
	s_mov_b64 s[6:7], -1
	global_store_dwordx2 v[4:5], v[2:3], off
	s_cbranch_vccnz .LBB0_754
	s_andn2_b64 vcc, exec, s[8:9]
	s_cbranch_vccnz .LBB0_753
	s_barrier
	s_branch .LBB0_753

.LBB0_1960:
	s_nop 15
	s_nop 15
	s_nop 15
	s_mov_b32 s98, 0x4a000000
	v_lshl_add_u32 v6, s61, 8, v173
	v_mul_f32_e32 v4, 0xb9b8aa3b, v158
	v_exp_f32_e32 v10, v4
	v_mul_f32_e32 v11, 0xb9b8aa3b, v159
	v_exp_f32_e32 v13, v11
	v_fma_f32 v10, v10, s98, s98
	v_rcp_f32_e32 v10, v10
	v_lshl_or_b32 v2, s60, 7, v193
	v_mov_b64_e32 v[4:5], s[8:9]
	v_ashrrev_i32_e32 v3, 31, v2
	v_mul_f32_e32 v11, v158, v10
	v_fma_f32 v7, v13, s98, s98
	v_rcp_f32_e32 v7, v7
	v_mul_f32_e32 v14, 0xb9b8aa3b, v160
	v_exp_f32_e32 v14, v14
	v_mad_i64_i32 v[8:9], s[22:23], v6, s46, v[4:5]
	v_mul_f32_e32 v15, v154, v11
	v_mul_f32_e32 v11, v159, v7
	v_fma_f32 v7, v14, s98, s98
	v_mul_f32_e32 v14, 0xb9b8aa3b, v161
	v_rcp_f32_e32 v7, v7
	v_exp_f32_e32 v14, v14
	v_lshl_add_u64 v[8:9], v[8:9], 0, v[2:3]
	v_mul_f32_e32 v16, v155, v11
	v_mul_f32_e32 v11, v160, v7
	v_fma_f32 v7, v14, s98, s98
	v_rcp_f32_e32 v7, v7
	s_andn2_b64 vcc, exec, s[4:5]
	v_mul_f32_e32 v13, v156, v11
	v_mul_f32_e32 v11, v161, v7
	v_mul_f32_e32 v10, 0xb9b8aa3b, v150
	v_exp_f32_e32 v12, v10
	v_med3_f32 v13, v13, s47, v197
	v_mul_f32_e32 v14, v157, v11
	v_fma_f32 v10, v12, s98, s98
	v_mul_f32_e32 v11, 0xb9b8aa3b, v151
	v_rcp_f32_e32 v10, v10
	v_exp_f32_e32 v17, v11
	v_med3_f32 v14, v14, s47, v197
	s_mov_b64 s[4:5], -1
	v_mul_f32_e32 v11, v150, v10
	v_fma_f32 v7, v17, s98, s98
	v_rcp_f32_e32 v7, v7
	v_mul_f32_e32 v18, 0xb9b8aa3b, v152
	v_exp_f32_e32 v18, v18
	s_nop 0
	v_mul_f32_e32 v19, v146, v11
	v_mul_f32_e32 v11, v151, v7
	v_fma_f32 v7, v18, s98, s98
	v_mul_f32_e32 v18, 0xb9b8aa3b, v153
	v_rcp_f32_e32 v7, v7
	v_exp_f32_e32 v18, v18
	s_nop 0
	v_mul_f32_e32 v20, v147, v11
	v_mul_f32_e32 v11, v152, v7
	v_fma_f32 v7, v18, s98, s98
	v_rcp_f32_e32 v7, v7
	s_nop 0
	v_mul_f32_e32 v17, v148, v11
	v_mul_f32_e32 v11, v153, v7
	v_med3_f32 v12, v16, s47, v197
	v_mul_f32_e32 v7, v149, v11
	v_med3_f32 v11, v15, s47, v197
	v_mov_b32_e32 v10, v169
	v_cvt_pk_fp8_f32 v10, v11, v12
	v_med3_f32 v12, v19, s47, v197
	v_med3_f32 v15, v20, s47, v197
	v_mov_b32_e32 v11, v169
	v_cvt_pk_fp8_f32 v11, v12, v15
	v_med3_f32 v12, v17, s47, v197
	v_med3_f32 v7, v7, s47, v197
	v_cvt_pk_fp8_f32 v10, v13, v14 op_sel:[0,0,1]
	v_cvt_pk_fp8_f32 v11, v12, v7 op_sel:[0,0,1]
	v_mul_f32_e32 v12, 0xb9b8aa3b, v142
	v_exp_f32_e32 v12, v12
	global_store_dwordx2 v[8:9], v[10:11], off
	v_mul_f32_e32 v9, 0xb9b8aa3b, v143
	v_fma_f32 v8, v12, s98, s98
	v_rcp_f32_e32 v8, v8
	v_exp_f32_e32 v12, v9
	v_or_b32_e32 v10, 16, v6
	v_mul_f32_e32 v9, v142, v8
	v_fma_f32 v7, v12, s98, s98
	v_rcp_f32_e32 v7, v7
	v_mul_f32_e32 v13, 0xb9b8aa3b, v144
	v_exp_f32_e32 v13, v13
	s_nop 0
	v_mul_f32_e32 v14, v138, v9
	v_mul_f32_e32 v9, v143, v7
	v_fma_f32 v7, v13, s98, s98
	v_mul_f32_e32 v13, 0xb9b8aa3b, v145
	v_rcp_f32_e32 v7, v7
	v_exp_f32_e32 v13, v13
	s_nop 0
	v_mul_f32_e32 v15, v139, v9
	v_mul_f32_e32 v9, v144, v7
	v_fma_f32 v7, v13, s98, s98
	v_rcp_f32_e32 v7, v7
	s_nop 0
	v_mul_f32_e32 v12, v140, v9
	v_mul_f32_e32 v9, v145, v7
	v_mul_f32_e32 v8, 0xb9b8aa3b, v134
	v_exp_f32_e32 v11, v8
	v_med3_f32 v12, v12, s47, v197
	v_mul_f32_e32 v13, v141, v9
	v_fma_f32 v8, v11, s98, s98
	v_mul_f32_e32 v9, 0xb9b8aa3b, v135
	v_rcp_f32_e32 v8, v8
	v_exp_f32_e32 v16, v9
	v_med3_f32 v13, v13, s47, v197
	v_mul_f32_e32 v9, v134, v8
	v_fma_f32 v7, v16, s98, s98
	v_rcp_f32_e32 v7, v7
	v_mul_f32_e32 v17, 0xb9b8aa3b, v136
	v_exp_f32_e32 v17, v17
	s_nop 0
	v_mul_f32_e32 v18, v130, v9
	v_mul_f32_e32 v9, v135, v7
	v_fma_f32 v7, v17, s98, s98
	v_mul_f32_e32 v17, 0xb9b8aa3b, v137
	v_rcp_f32_e32 v7, v7
	v_exp_f32_e32 v17, v17
	s_nop 0
	v_mul_f32_e32 v19, v131, v9
	v_mul_f32_e32 v9, v136, v7
	v_fma_f32 v7, v17, s98, s98
	v_rcp_f32_e32 v7, v7
	s_nop 0
	v_mul_f32_e32 v16, v132, v9
	v_mul_f32_e32 v9, v137, v7
	v_med3_f32 v11, v15, s47, v197
	v_mul_f32_e32 v7, v133, v9
	v_med3_f32 v9, v14, s47, v197
	v_mov_b32_e32 v8, v169
	v_cvt_pk_fp8_f32 v8, v9, v11
	v_med3_f32 v11, v18, s47, v197
	v_med3_f32 v14, v19, s47, v197
	v_mov_b32_e32 v9, v169
	v_cvt_pk_fp8_f32 v9, v11, v14
	v_med3_f32 v11, v16, s47, v197
	v_med3_f32 v7, v7, s47, v197
	v_cvt_pk_fp8_f32 v8, v12, v13 op_sel:[0,0,1]
	v_cvt_pk_fp8_f32 v9, v11, v7 op_sel:[0,0,1]
	v_mad_i64_i32 v[10:11], s[22:23], v10, s46, v[4:5]
	v_lshl_add_u64 v[10:11], v[10:11], 0, v[2:3]
	global_store_dwordx2 v[10:11], v[8:9], off
	v_mul_f32_e32 v8, 0xb9b8aa3b, v126
	v_exp_f32_e32 v10, v8
	v_mul_f32_e32 v11, 0xb9b8aa3b, v127
	v_exp_f32_e32 v13, v11
	v_fma_f32 v10, v10, s98, s98
	v_rcp_f32_e32 v10, v10
	v_or_b32_e32 v8, 32, v6
	v_mad_i64_i32 v[8:9], s[22:23], v8, s46, v[4:5]
	v_mul_f32_e32 v11, v126, v10
	v_fma_f32 v7, v13, s98, s98
	v_rcp_f32_e32 v7, v7
	v_mul_f32_e32 v14, 0xb9b8aa3b, v128
	v_exp_f32_e32 v14, v14
	v_lshl_add_u64 v[8:9], v[8:9], 0, v[2:3]
	v_mul_f32_e32 v15, v122, v11
	v_mul_f32_e32 v11, v127, v7
	v_fma_f32 v7, v14, s98, s98
	v_mul_f32_e32 v14, 0xb9b8aa3b, v129
	v_rcp_f32_e32 v7, v7
	v_exp_f32_e32 v14, v14
	s_nop 0
	v_mul_f32_e32 v16, v123, v11
	v_mul_f32_e32 v11, v128, v7
	v_fma_f32 v7, v14, s98, s98
	v_rcp_f32_e32 v7, v7
	s_nop 0
	v_mul_f32_e32 v13, v124, v11
	v_mul_f32_e32 v11, v129, v7
	v_mul_f32_e32 v10, 0xb9b8aa3b, v118
	v_exp_f32_e32 v12, v10
	v_med3_f32 v13, v13, s47, v197
	v_mul_f32_e32 v14, v125, v11
	v_fma_f32 v10, v12, s98, s98
	v_mul_f32_e32 v11, 0xb9b8aa3b, v119
	v_rcp_f32_e32 v10, v10
	v_exp_f32_e32 v17, v11
	v_med3_f32 v14, v14, s47, v197
	v_mul_f32_e32 v11, v118, v10
	v_fma_f32 v7, v17, s98, s98
	v_rcp_f32_e32 v7, v7
	v_mul_f32_e32 v18, 0xb9b8aa3b, v120
	v_exp_f32_e32 v18, v18
	s_nop 0
	v_mul_f32_e32 v19, v114, v11
	v_mul_f32_e32 v11, v119, v7
	v_fma_f32 v7, v18, s98, s98
	v_mul_f32_e32 v18, 0xb9b8aa3b, v121
	v_rcp_f32_e32 v7, v7
	v_exp_f32_e32 v18, v18
	s_nop 0
	v_mul_f32_e32 v20, v115, v11
	v_mul_f32_e32 v11, v120, v7
	v_fma_f32 v7, v18, s98, s98
	v_rcp_f32_e32 v7, v7
	s_nop 0
	v_mul_f32_e32 v17, v116, v11
	v_mul_f32_e32 v11, v121, v7
	v_med3_f32 v12, v16, s47, v197
	v_mul_f32_e32 v7, v117, v11
	v_med3_f32 v11, v15, s47, v197
	v_mov_b32_e32 v10, v169
	v_cvt_pk_fp8_f32 v10, v11, v12
	v_med3_f32 v12, v19, s47, v197
	v_med3_f32 v15, v20, s47, v197
	v_mov_b32_e32 v11, v169
	v_cvt_pk_fp8_f32 v11, v12, v15
	v_med3_f32 v12, v17, s47, v197
	v_med3_f32 v7, v7, s47, v197
	v_cvt_pk_fp8_f32 v10, v13, v14 op_sel:[0,0,1]
	v_cvt_pk_fp8_f32 v11, v12, v7 op_sel:[0,0,1]
	v_mul_f32_e32 v12, 0xb9b8aa3b, v110
	v_exp_f32_e32 v12, v12
	global_store_dwordx2 v[8:9], v[10:11], off
	v_mul_f32_e32 v9, 0xb9b8aa3b, v111
	v_fma_f32 v8, v12, s98, s98
	v_rcp_f32_e32 v8, v8
	v_exp_f32_e32 v12, v9
	v_or_b32_e32 v10, 48, v6
	v_mul_f32_e32 v9, v110, v8
	v_fma_f32 v7, v12, s98, s98
	v_rcp_f32_e32 v7, v7
	v_mul_f32_e32 v13, 0xb9b8aa3b, v112
	v_exp_f32_e32 v13, v13
	s_nop 0
	v_mul_f32_e32 v14, v106, v9
	v_mul_f32_e32 v9, v111, v7
	v_fma_f32 v7, v13, s98, s98
	v_mul_f32_e32 v13, 0xb9b8aa3b, v113
	v_rcp_f32_e32 v7, v7
	v_exp_f32_e32 v13, v13
	s_nop 0
	v_mul_f32_e32 v15, v107, v9
	v_mul_f32_e32 v9, v112, v7
	v_fma_f32 v7, v13, s98, s98
	v_rcp_f32_e32 v7, v7
	s_nop 0
	v_mul_f32_e32 v12, v108, v9
	v_mul_f32_e32 v9, v113, v7
	v_mul_f32_e32 v8, 0xb9b8aa3b, v102
	v_exp_f32_e32 v11, v8
	v_med3_f32 v12, v12, s47, v197
	v_mul_f32_e32 v13, v109, v9
	v_fma_f32 v8, v11, s98, s98
	v_mul_f32_e32 v9, 0xb9b8aa3b, v103
	v_rcp_f32_e32 v8, v8
	v_exp_f32_e32 v16, v9
	v_med3_f32 v13, v13, s47, v197
	v_mul_f32_e32 v9, v102, v8
	v_fma_f32 v7, v16, s98, s98
	v_rcp_f32_e32 v7, v7
	v_mul_f32_e32 v17, 0xb9b8aa3b, v104
	v_exp_f32_e32 v17, v17
	s_nop 0
	v_mul_f32_e32 v18, v98, v9
	v_mul_f32_e32 v9, v103, v7
	v_fma_f32 v7, v17, s98, s98
	v_mul_f32_e32 v17, 0xb9b8aa3b, v105
	v_rcp_f32_e32 v7, v7
	v_exp_f32_e32 v17, v17
	s_nop 0
	v_mul_f32_e32 v19, v99, v9
	v_mul_f32_e32 v9, v104, v7
	v_fma_f32 v7, v17, s98, s98
	v_rcp_f32_e32 v7, v7
	s_nop 0
	v_mul_f32_e32 v16, v100, v9
	v_mul_f32_e32 v9, v105, v7
	v_med3_f32 v11, v15, s47, v197
	v_mul_f32_e32 v7, v101, v9
	v_med3_f32 v9, v14, s47, v197
	v_mov_b32_e32 v8, v169
	v_cvt_pk_fp8_f32 v8, v9, v11
	v_med3_f32 v11, v18, s47, v197
	v_med3_f32 v14, v19, s47, v197
	v_mov_b32_e32 v9, v169
	v_cvt_pk_fp8_f32 v9, v11, v14
	v_med3_f32 v11, v16, s47, v197
	v_med3_f32 v7, v7, s47, v197
	v_cvt_pk_fp8_f32 v8, v12, v13 op_sel:[0,0,1]
	v_cvt_pk_fp8_f32 v9, v11, v7 op_sel:[0,0,1]
	v_mad_i64_i32 v[10:11], s[22:23], v10, s46, v[4:5]
	v_lshl_add_u64 v[10:11], v[10:11], 0, v[2:3]
	global_store_dwordx2 v[10:11], v[8:9], off
	v_mul_f32_e32 v8, 0xb9b8aa3b, v94
	v_exp_f32_e32 v10, v8
	v_mul_f32_e32 v11, 0xb9b8aa3b, v95
	v_exp_f32_e32 v13, v11
	v_fma_f32 v10, v10, s98, s98
	v_rcp_f32_e32 v10, v10
	v_add_u32_e32 v8, 0x80, v6
	v_mad_i64_i32 v[8:9], s[22:23], v8, s46, v[4:5]
	v_mul_f32_e32 v11, v94, v10
	v_fma_f32 v7, v13, s98, s98
	v_rcp_f32_e32 v7, v7
	v_mul_f32_e32 v14, 0xb9b8aa3b, v96
	v_exp_f32_e32 v14, v14
	v_lshl_add_u64 v[8:9], v[8:9], 0, v[2:3]
	v_mul_f32_e32 v15, v90, v11
	v_mul_f32_e32 v11, v95, v7
	v_fma_f32 v7, v14, s98, s98
	v_mul_f32_e32 v14, 0xb9b8aa3b, v97
	v_rcp_f32_e32 v7, v7
	v_exp_f32_e32 v14, v14
	s_nop 0
	v_mul_f32_e32 v16, v91, v11
	v_mul_f32_e32 v11, v96, v7
	v_fma_f32 v7, v14, s98, s98
	v_rcp_f32_e32 v7, v7
	s_nop 0
	v_mul_f32_e32 v13, v92, v11
	v_mul_f32_e32 v11, v97, v7
	v_mul_f32_e32 v10, 0xb9b8aa3b, v86
	v_exp_f32_e32 v12, v10
	v_med3_f32 v13, v13, s47, v197
	v_mul_f32_e32 v14, v93, v11
	v_fma_f32 v10, v12, s98, s98
	v_mul_f32_e32 v11, 0xb9b8aa3b, v87
	v_rcp_f32_e32 v10, v10
	v_exp_f32_e32 v17, v11
	v_med3_f32 v14, v14, s47, v197
	v_mul_f32_e32 v11, v86, v10
	v_fma_f32 v7, v17, s98, s98
	v_rcp_f32_e32 v7, v7
	v_mul_f32_e32 v18, 0xb9b8aa3b, v88
	v_exp_f32_e32 v18, v18
	s_nop 0
	v_mul_f32_e32 v19, v82, v11
	v_mul_f32_e32 v11, v87, v7
	v_fma_f32 v7, v18, s98, s98
	v_mul_f32_e32 v18, 0xb9b8aa3b, v89
	v_rcp_f32_e32 v7, v7
	v_exp_f32_e32 v18, v18
	s_nop 0
	v_mul_f32_e32 v20, v83, v11
	v_mul_f32_e32 v11, v88, v7
	v_fma_f32 v7, v18, s98, s98
	v_rcp_f32_e32 v7, v7
	s_nop 0
	v_mul_f32_e32 v17, v84, v11
	v_mul_f32_e32 v11, v89, v7
	v_med3_f32 v12, v16, s47, v197
	v_mul_f32_e32 v7, v85, v11
	v_med3_f32 v11, v15, s47, v197
	v_mov_b32_e32 v10, v169
	v_cvt_pk_fp8_f32 v10, v11, v12
	v_med3_f32 v12, v19, s47, v197
	v_med3_f32 v15, v20, s47, v197
	v_mov_b32_e32 v11, v169
	v_cvt_pk_fp8_f32 v11, v12, v15
	v_med3_f32 v12, v17, s47, v197
	v_med3_f32 v7, v7, s47, v197
	v_cvt_pk_fp8_f32 v10, v13, v14 op_sel:[0,0,1]
	v_cvt_pk_fp8_f32 v11, v12, v7 op_sel:[0,0,1]
	v_mul_f32_e32 v12, 0xb9b8aa3b, v78
	v_exp_f32_e32 v12, v12
	global_store_dwordx2 v[8:9], v[10:11], off
	v_mul_f32_e32 v9, 0xb9b8aa3b, v79
	v_fma_f32 v8, v12, s98, s98
	v_rcp_f32_e32 v8, v8
	v_exp_f32_e32 v12, v9
	v_add_u32_e32 v10, 0x90, v6
	v_mul_f32_e32 v9, v78, v8
	v_fma_f32 v7, v12, s98, s98
	v_rcp_f32_e32 v7, v7
	v_mul_f32_e32 v13, 0xb9b8aa3b, v80
	v_exp_f32_e32 v13, v13
	s_nop 0
	v_mul_f32_e32 v14, v74, v9
	v_mul_f32_e32 v9, v79, v7
	v_fma_f32 v7, v13, s98, s98
	v_mul_f32_e32 v13, 0xb9b8aa3b, v81
	v_rcp_f32_e32 v7, v7
	v_exp_f32_e32 v13, v13
	s_nop 0
	v_mul_f32_e32 v15, v75, v9
	v_mul_f32_e32 v9, v80, v7
	v_fma_f32 v7, v13, s98, s98
	v_rcp_f32_e32 v7, v7
	s_nop 0
	v_mul_f32_e32 v12, v76, v9
	v_mul_f32_e32 v9, v81, v7
	v_mul_f32_e32 v8, 0xb9b8aa3b, v70
	v_exp_f32_e32 v11, v8
	v_med3_f32 v12, v12, s47, v197
	v_mul_f32_e32 v13, v77, v9
	v_fma_f32 v8, v11, s98, s98
	v_mul_f32_e32 v9, 0xb9b8aa3b, v71
	v_rcp_f32_e32 v8, v8
	v_exp_f32_e32 v16, v9
	v_med3_f32 v13, v13, s47, v197
	v_mul_f32_e32 v9, v70, v8
	v_fma_f32 v7, v16, s98, s98
	v_rcp_f32_e32 v7, v7
	v_mul_f32_e32 v17, 0xb9b8aa3b, v72
	v_exp_f32_e32 v17, v17
	s_nop 0
	v_mul_f32_e32 v18, v66, v9
	v_mul_f32_e32 v9, v71, v7
	v_fma_f32 v7, v17, s98, s98
	v_mul_f32_e32 v17, 0xb9b8aa3b, v73
	v_rcp_f32_e32 v7, v7
	v_exp_f32_e32 v17, v17
	s_nop 0
	v_mul_f32_e32 v19, v67, v9
	v_mul_f32_e32 v9, v72, v7
	v_fma_f32 v7, v17, s98, s98
	v_rcp_f32_e32 v7, v7
	s_nop 0
	v_mul_f32_e32 v16, v68, v9
	v_mul_f32_e32 v9, v73, v7
	v_med3_f32 v11, v15, s47, v197
	v_mul_f32_e32 v7, v69, v9
	v_med3_f32 v9, v14, s47, v197
	v_mov_b32_e32 v8, v169
	v_cvt_pk_fp8_f32 v8, v9, v11
	v_med3_f32 v11, v18, s47, v197
	v_med3_f32 v14, v19, s47, v197
	v_mov_b32_e32 v9, v169
	v_cvt_pk_fp8_f32 v9, v11, v14
	v_med3_f32 v11, v16, s47, v197
	v_med3_f32 v7, v7, s47, v197
	v_cvt_pk_fp8_f32 v8, v12, v13 op_sel:[0,0,1]
	v_cvt_pk_fp8_f32 v9, v11, v7 op_sel:[0,0,1]
	v_mad_i64_i32 v[10:11], s[22:23], v10, s46, v[4:5]
	v_lshl_add_u64 v[10:11], v[10:11], 0, v[2:3]
	global_store_dwordx2 v[10:11], v[8:9], off
	v_mul_f32_e32 v8, 0xb9b8aa3b, v62
	v_exp_f32_e32 v10, v8
	v_mul_f32_e32 v11, 0xb9b8aa3b, v63
	v_exp_f32_e32 v13, v11
	v_fma_f32 v10, v10, s98, s98
	v_rcp_f32_e32 v10, v10
	v_add_u32_e32 v8, 0xa0, v6
	v_mad_i64_i32 v[8:9], s[22:23], v8, s46, v[4:5]
	v_mul_f32_e32 v11, v62, v10
	v_fma_f32 v7, v13, s98, s98
	v_rcp_f32_e32 v7, v7
	v_mul_f32_e32 v14, 0xb9b8aa3b, v64
	v_exp_f32_e32 v14, v14
	v_lshl_add_u64 v[8:9], v[8:9], 0, v[2:3]
	v_mul_f32_e32 v15, v58, v11
	v_mul_f32_e32 v11, v63, v7
	v_fma_f32 v7, v14, s98, s98
	v_mul_f32_e32 v14, 0xb9b8aa3b, v65
	v_rcp_f32_e32 v7, v7
	v_exp_f32_e32 v14, v14
	s_nop 0
	v_mul_f32_e32 v16, v59, v11
	v_mul_f32_e32 v11, v64, v7
	v_fma_f32 v7, v14, s98, s98
	v_rcp_f32_e32 v7, v7
	s_nop 0
	v_mul_f32_e32 v13, v60, v11
	v_mul_f32_e32 v11, v65, v7
	v_mul_f32_e32 v10, 0xb9b8aa3b, v54
	v_exp_f32_e32 v12, v10
	v_med3_f32 v13, v13, s47, v197
	v_mul_f32_e32 v14, v61, v11
	v_fma_f32 v10, v12, s98, s98
	v_mul_f32_e32 v11, 0xb9b8aa3b, v55
	v_rcp_f32_e32 v10, v10
	v_exp_f32_e32 v17, v11
	v_med3_f32 v14, v14, s47, v197
	v_mul_f32_e32 v11, v54, v10
	v_fma_f32 v7, v17, s98, s98
	v_rcp_f32_e32 v7, v7
	v_mul_f32_e32 v18, 0xb9b8aa3b, v56
	v_exp_f32_e32 v18, v18
	s_nop 0
	v_mul_f32_e32 v19, v50, v11
	v_mul_f32_e32 v11, v55, v7
	v_fma_f32 v7, v18, s98, s98
	v_mul_f32_e32 v18, 0xb9b8aa3b, v57
	v_rcp_f32_e32 v7, v7
	v_exp_f32_e32 v18, v18
	s_nop 0
	v_mul_f32_e32 v20, v51, v11
	v_mul_f32_e32 v11, v56, v7
	v_fma_f32 v7, v18, s98, s98
	v_rcp_f32_e32 v7, v7
	s_nop 0
	v_mul_f32_e32 v17, v52, v11
	v_mul_f32_e32 v11, v57, v7
	v_med3_f32 v12, v16, s47, v197
	v_mul_f32_e32 v7, v53, v11
	v_med3_f32 v11, v15, s47, v197
	v_mov_b32_e32 v10, v169
	v_cvt_pk_fp8_f32 v10, v11, v12
	v_med3_f32 v12, v19, s47, v197
	v_med3_f32 v15, v20, s47, v197
	v_mov_b32_e32 v11, v169
	v_cvt_pk_fp8_f32 v11, v12, v15
	v_med3_f32 v12, v17, s47, v197
	v_med3_f32 v7, v7, s47, v197
	v_cvt_pk_fp8_f32 v10, v13, v14 op_sel:[0,0,1]
	v_cvt_pk_fp8_f32 v11, v12, v7 op_sel:[0,0,1]
	v_mul_f32_e32 v12, 0xb9b8aa3b, v46
	v_exp_f32_e32 v12, v12
	global_store_dwordx2 v[8:9], v[10:11], off
	v_mul_f32_e32 v10, 0xb9b8aa3b, v47
	v_exp_f32_e32 v10, v10
	v_add_u32_e32 v8, 0xb0, v6
	v_fma_f32 v6, v12, s98, s98
	v_rcp_f32_e32 v6, v6
	v_fma_f32 v10, v10, s98, s98
	v_rcp_f32_e32 v10, v10
	v_mul_f32_e32 v12, 0xb9b8aa3b, v48
	v_exp_f32_e32 v12, v12
	v_mul_f32_e32 v7, v46, v6
	v_mad_i64_i32 v[4:5], s[22:23], v8, s46, v[4:5]
	v_mul_f32_e32 v13, v42, v7
	v_mul_f32_e32 v7, v47, v10
	v_fma_f32 v9, v12, s98, s98
	v_mul_f32_e32 v12, 0xb9b8aa3b, v49
	v_exp_f32_e32 v12, v12
	v_rcp_f32_e32 v9, v9
	v_lshl_add_u64 v[2:3], v[4:5], 0, v[2:3]
	v_mul_f32_e32 v14, v43, v7
	v_fma_f32 v6, v12, s98, s98
	v_mul_f32_e32 v7, v48, v9
	v_rcp_f32_e32 v9, v6
	s_nop 0
	v_mul_f32_e32 v11, v44, v7
	v_mul_f32_e32 v7, v49, v9
	v_mul_f32_e32 v6, 0xb9b8aa3b, v38
	v_exp_f32_e32 v10, v6
	v_med3_f32 v11, v11, s47, v197
	v_mul_f32_e32 v12, v45, v7
	v_fma_f32 v6, v10, s98, s98
	v_mul_f32_e32 v7, 0xb9b8aa3b, v39
	v_rcp_f32_e32 v6, v6
	v_exp_f32_e32 v15, v7
	v_med3_f32 v12, v12, s47, v197
	v_mul_f32_e32 v7, v38, v6
	v_fma_f32 v9, v15, s98, s98
	v_rcp_f32_e32 v9, v9
	v_mul_f32_e32 v16, 0xb9b8aa3b, v40
	v_exp_f32_e32 v16, v16
	s_nop 0
	v_mul_f32_e32 v17, v34, v7
	v_mul_f32_e32 v7, v39, v9
	v_fma_f32 v9, v16, s98, s98
	v_mul_f32_e32 v16, 0xb9b8aa3b, v41
	v_exp_f32_e32 v16, v16
	v_rcp_f32_e32 v9, v9
	s_nop 0
	v_mul_f32_e32 v18, v35, v7
	v_fma_f32 v6, v16, s98, s98
	v_mul_f32_e32 v7, v40, v9
	v_rcp_f32_e32 v9, v6
	s_nop 0
	v_mul_f32_e32 v15, v36, v7
	v_mul_f32_e32 v7, v41, v9
	v_med3_f32 v10, v14, s47, v197
	v_mul_f32_e32 v9, v37, v7
	v_med3_f32 v7, v13, s47, v197
	v_mov_b32_e32 v6, v169
	v_cvt_pk_fp8_f32 v6, v7, v10
	v_med3_f32 v10, v17, s47, v197
	v_med3_f32 v13, v18, s47, v197
	v_mov_b32_e32 v7, v169
	v_cvt_pk_fp8_f32 v7, v10, v13
	v_med3_f32 v10, v15, s47, v197
	v_med3_f32 v9, v9, s47, v197
	v_cvt_pk_fp8_f32 v6, v11, v12 op_sel:[0,0,1]
	v_cvt_pk_fp8_f32 v7, v10, v9 op_sel:[0,0,1]
	global_store_dwordx2 v[2:3], v[6:7], off
	s_cbranch_vccnz .LBB0_1953
	s_andn2_b64 vcc, exec, s[6:7]
	s_cbranch_vccnz .LBB0_1952
	s_barrier
	s_branch .LBB0_1952
